# RG-LRU: static priority raise for waves 4-7 combined with the gate tile fetched by LDS-DMA in the backward pass
# baseline (speedup 1.0000x reference)
.Lmylru_w1_9:
	v_lshrrev_b32_e32 v184, 11, v210
	v_and_b32_e32 v185, 0x7ff, v210
	v_lshl_add_u32 v184, v184, 7, v185
	v_add_u32_e32 v184, 0x20800, v184
	ds_read_u16 v128, v184
	ds_read_u16 v129, v184 offset:128
	ds_read_u16 v130, v184 offset:256
	ds_read_u16 v131, v184 offset:384
	ds_read_u16 v132, v184 offset:2048
	ds_read_u16 v133, v184 offset:2176
	ds_read_u16 v134, v184 offset:2304
	ds_read_u16 v135, v184 offset:2432
	ds_read_u16 v136, v184 offset:4096
	ds_read_u16 v137, v184 offset:4224
	ds_read_u16 v138, v184 offset:4352
	ds_read_u16 v139, v184 offset:4480
	ds_read_u16 v140, v184 offset:6144
	ds_read_u16 v141, v184 offset:6272
	ds_read_u16 v142, v184 offset:6400
	ds_read_u16 v143, v184 offset:6528
	s_waitcnt lgkmcnt(0)
	v_lshlrev_b32_e32 v178, 16, v247
	v_add_f32_e32 v144, v144, v178
	v_lshlrev_b32_e32 v128, 16, v128
	v_mul_f32_e32 v144, v144, v128
	v_cvt_pk_bf16_f32 v144, v144, v144
	v_and_b32_e32 v179, 0xffff0000, v247
	v_add_f32_e32 v145, v145, v179
	v_lshlrev_b32_e32 v129, 16, v129
	v_mul_f32_e32 v145, v145, v129
	v_cvt_pk_bf16_f32 v145, v145, v145
	v_lshlrev_b32_e32 v180, 16, v248
	v_add_f32_e32 v146, v146, v180
	v_lshlrev_b32_e32 v130, 16, v130
	v_mul_f32_e32 v146, v146, v130
	v_cvt_pk_bf16_f32 v146, v146, v146
	v_and_b32_e32 v181, 0xffff0000, v248
	v_add_f32_e32 v147, v147, v181
	v_lshlrev_b32_e32 v131, 16, v131
	v_mul_f32_e32 v147, v147, v131
	v_cvt_pk_bf16_f32 v147, v147, v147
	v_lshlrev_b32_e32 v178, 16, v249
	v_add_f32_e32 v148, v148, v178
	v_lshlrev_b32_e32 v132, 16, v132
	v_mul_f32_e32 v148, v148, v132
	v_cvt_pk_bf16_f32 v148, v148, v148
	v_and_b32_e32 v179, 0xffff0000, v249
	v_add_f32_e32 v149, v149, v179
	v_lshlrev_b32_e32 v133, 16, v133
	v_mul_f32_e32 v149, v149, v133
	v_cvt_pk_bf16_f32 v149, v149, v149
	v_lshlrev_b32_e32 v180, 16, v250
	v_add_f32_e32 v150, v150, v180
	v_lshlrev_b32_e32 v134, 16, v134
	v_mul_f32_e32 v150, v150, v134
	v_cvt_pk_bf16_f32 v150, v150, v150
	v_and_b32_e32 v181, 0xffff0000, v250
	v_add_f32_e32 v151, v151, v181
	v_lshlrev_b32_e32 v135, 16, v135
	v_mul_f32_e32 v151, v151, v135
	v_cvt_pk_bf16_f32 v151, v151, v151
	v_lshlrev_b32_e32 v178, 16, v251
	v_add_f32_e32 v152, v152, v178
	v_lshlrev_b32_e32 v136, 16, v136
	v_mul_f32_e32 v152, v152, v136
	v_cvt_pk_bf16_f32 v152, v152, v152
	v_and_b32_e32 v179, 0xffff0000, v251
	v_add_f32_e32 v153, v153, v179
	v_lshlrev_b32_e32 v137, 16, v137
	v_mul_f32_e32 v153, v153, v137
	v_cvt_pk_bf16_f32 v153, v153, v153
	v_lshlrev_b32_e32 v180, 16, v252
	v_add_f32_e32 v154, v154, v180
	v_lshlrev_b32_e32 v138, 16, v138
	v_mul_f32_e32 v154, v154, v138
	v_cvt_pk_bf16_f32 v154, v154, v154
	v_and_b32_e32 v181, 0xffff0000, v252
	v_add_f32_e32 v155, v155, v181
	v_lshlrev_b32_e32 v139, 16, v139
	v_mul_f32_e32 v155, v155, v139
	v_cvt_pk_bf16_f32 v155, v155, v155
	v_lshlrev_b32_e32 v178, 16, v253
	v_add_f32_e32 v156, v156, v178
	v_lshlrev_b32_e32 v140, 16, v140
	v_mul_f32_e32 v156, v156, v140
	v_cvt_pk_bf16_f32 v156, v156, v156
	v_and_b32_e32 v179, 0xffff0000, v253
	v_add_f32_e32 v157, v157, v179
	v_lshlrev_b32_e32 v141, 16, v141
	v_mul_f32_e32 v157, v157, v141
	v_cvt_pk_bf16_f32 v157, v157, v157
	v_lshlrev_b32_e32 v180, 16, v254
	v_add_f32_e32 v158, v158, v180
	v_lshlrev_b32_e32 v142, 16, v142
	v_mul_f32_e32 v158, v158, v142
	v_cvt_pk_bf16_f32 v158, v158, v158
	v_and_b32_e32 v181, 0xffff0000, v254
	v_add_f32_e32 v159, v159, v181
	v_lshlrev_b32_e32 v143, 16, v143
	v_mul_f32_e32 v159, v159, v143
	v_cvt_pk_bf16_f32 v159, v159, v159
	v_add_u32_e32 v182, 0x0, v210
	v_add_u32_e32 v183, 0x1000, v182
	global_store_short v182, v144, s[42:43]
	global_store_short v182, v145, s[42:43] offset:2048
	global_store_short v183, v146, s[42:43]
	global_store_short v183, v147, s[42:43] offset:2048
	v_add_u32_e32 v182, 0x8000, v210
	v_add_u32_e32 v183, 0x1000, v182
	global_store_short v182, v148, s[42:43]
	global_store_short v182, v149, s[42:43] offset:2048
	global_store_short v183, v150, s[42:43]
	global_store_short v183, v151, s[42:43] offset:2048
	v_add_u32_e32 v182, 0x10000, v210
	v_add_u32_e32 v183, 0x1000, v182
	global_store_short v182, v152, s[42:43]
	global_store_short v182, v153, s[42:43] offset:2048
	global_store_short v183, v154, s[42:43]
	global_store_short v183, v155, s[42:43] offset:2048
	v_add_u32_e32 v182, 0x18000, v210
	v_add_u32_e32 v183, 0x1000, v182
	global_store_short v182, v156, s[42:43]
	global_store_short v182, v157, s[42:43] offset:2048
	global_store_short v183, v158, s[42:43]
	global_store_short v183, v159, s[42:43] offset:2048
	s_add_i32 s13, s13, 1
	s_add_i32 s60, s60, -1
	s_cmp_lg_u32 s60, 0
	s_cbranch_scc1 .Lmylru_loop_1
	s_waitcnt vmcnt(0) lgkmcnt(0)
	s_setprio 0
